# NSA tile loop header on a 64-byte boundary (other loops at their baseline offsets)
# baseline (speedup 1.0000x reference)
.LBB0_2419:
	s_lshl_b32 s2, s2, 13
	s_add_i32 s76, s2, 0
	s_add_i32 s76, s76, 0x10000
	s_andn2_b64 vcc, exec, s[8:9]
	v_lshlrev_b32_e32 v134, 2, v162
	s_cbranch_vccnz .LBB0_2468
	v_or_b32_e32 v6, 32, v168
	v_cmp_gt_i32_e64 s[40:41], v6, v2
	v_cmp_lt_i32_e64 s[42:43], v6, v2
	v_or_b32_e32 v6, 34, v168
	v_cmp_gt_i32_e64 s[44:45], v6, v2
	v_or_b32_e32 v6, 35, v168
	v_cmp_gt_i32_e64 s[46:47], v6, v2
	v_or_b32_e32 v6, 40, v168
	v_cmp_gt_i32_e64 s[48:49], v6, v2
	v_or_b32_e32 v6, 41, v168
	v_cmp_gt_i32_e64 s[50:51], v6, v2
	v_or_b32_e32 v6, 42, v168
	v_cmp_gt_i32_e64 s[52:53], v6, v2
	v_or_b32_e32 v6, 43, v168
	v_cmp_gt_i32_e64 s[54:55], v6, v2
	v_or_b32_e32 v6, 48, v168
	v_cmp_gt_i32_e64 s[56:57], v6, v2
	v_or_b32_e32 v6, 49, v168
	v_cmp_gt_i32_e64 s[58:59], v6, v2
	v_or_b32_e32 v6, 50, v168
	v_cmp_gt_i32_e64 s[60:61], v6, v2
	v_or_b32_e32 v6, 51, v168
	v_cmp_gt_i32_e64 s[62:63], v6, v2
	v_or_b32_e32 v6, 56, v168
	v_cmp_gt_i32_e64 s[64:65], v6, v2
	v_or_b32_e32 v6, 57, v168
	v_cmp_gt_i32_e64 s[66:67], v6, v2
	v_or_b32_e32 v6, 58, v168
	v_cmp_gt_i32_e64 s[68:69], v6, v2
	v_or_b32_e32 v6, 59, v168
	v_cmp_gt_i32_e64 s[6:7], v168, v2
	v_cmp_lt_i32_e64 s[8:9], v168, v2
	v_cmp_gt_i32_e64 s[10:11], v135, v2
	v_cmp_gt_i32_e64 s[12:13], v169, v2
	v_cmp_gt_i32_e64 s[14:15], v170, v2
	v_cmp_gt_i32_e64 s[16:17], v171, v2
	v_cmp_gt_i32_e64 s[18:19], v172, v2
	v_cmp_gt_i32_e64 s[20:21], v173, v2
	v_cmp_gt_i32_e64 s[22:23], v174, v2
	v_cmp_gt_i32_e64 s[24:25], v175, v2
	v_cmp_gt_i32_e64 s[26:27], v176, v2
	v_cmp_gt_i32_e64 s[28:29], v177, v2
	v_cmp_gt_i32_e64 s[30:31], v178, v2
	v_cmp_gt_i32_e64 s[34:35], v179, v2
	v_cmp_gt_i32_e64 s[36:37], v180, v2
	v_cmp_gt_i32_e64 s[38:39], v181, v2
	v_cmp_gt_i32_e64 s[70:71], v6, v2
	s_min_u32 s2, s92, 8
	v_lshlrev_b32_e32 v2, 4, v4
	s_add_i32 s2, s92, s2
	v_and_b32_e32 v2, 0xc0, v2
	s_lshl_b32 s87, s2, 13
	v_lshl_or_b32 v2, v160, 8, v2
	v_readlane_b32 s2, v247, 4
	v_lshlrev_b32_e32 v5, 1, v4
	v_mov_b32_e32 v140, 0
	v_add_u32_e32 v185, s2, v2
	v_readlane_b32 s2, v247, 5
	s_movk_i32 s96, 0xc00
	s_add_i32 s91, s91, s92
	v_add_u32_e32 v187, s2, v2
	v_readlane_b32 s2, v247, 6
	s_add_i32 s93, s93, s3
	v_mov_b32_e32 v139, v131
	v_add_u32_e32 v188, s2, v2
	v_readlane_b32 s2, v247, 7
	s_mov_b32 s94, 2
	v_add_u32_e32 v183, s75, v134
	v_add_u32_e32 v189, s2, v2
	v_readlane_b32 s2, v247, 8
	v_add3_u32 v184, s76, v166, v134
	s_lshl_b32 s95, s92, 13
	v_add_u32_e32 v190, s2, v2
	v_readlane_b32 s2, v247, 9
	s_addk_i32 s87, 0x4000
	v_and_or_b32 v186, v5, 32, v3
	v_add_u32_e32 v191, s2, v2
	v_readlane_b32 s2, v247, 10
	s_add_i32 s86, s75, 0xc000
	s_mov_b32 s3, 0
	v_add_u32_e32 v192, s2, v2
	v_readlane_b32 s2, v247, 11
	v_mov_b32_e32 v202, 0
	v_mov_b32_e32 v3, v140
	v_add_u32_e32 v193, s2, v2
	v_readlane_b32 s2, v247, 12
	v_mov_b32_e32 v4, v140
	v_mov_b32_e32 v5, v140
	v_add_u32_e32 v194, s2, v2
	v_readlane_b32 s2, v247, 13
	v_mov_b32_e32 v6, v140
	v_mov_b32_e32 v7, v140
	v_add_u32_e32 v195, s2, v2
	v_readlane_b32 s2, v247, 14
	v_mov_b32_e32 v8, v140
	v_mov_b32_e32 v9, v140
	v_add_u32_e32 v196, s2, v2
	v_readlane_b32 s2, v247, 15
	v_mov_b32_e32 v10, v140
	v_mov_b32_e32 v11, v140
	v_add_u32_e32 v197, s2, v2
	v_readlane_b32 s2, v247, 16
	v_mov_b32_e32 v12, v140
	v_mov_b32_e32 v13, v140
	v_add_u32_e32 v198, s2, v2
	v_readlane_b32 s2, v247, 17
	v_mov_b32_e32 v14, v140
	v_mov_b32_e32 v15, v140
	v_add_u32_e32 v199, s2, v2
	v_readlane_b32 s2, v247, 21
	v_mov_b32_e32 v16, v140
	v_mov_b32_e32 v17, v140
	v_add_u32_e32 v200, s2, v2
	s_add_i32 s2, 0, 0x8000
	v_add_u32_e32 v201, s2, v2
	s_mov_b32 s2, 0
	v_mov_b32_e32 v2, 0
	v_mov_b32_e32 v18, 0
	v_mov_b32_e32 v19, v140
	v_mov_b32_e32 v20, v140
	v_mov_b32_e32 v21, v140
	v_mov_b32_e32 v22, v140
	v_mov_b32_e32 v23, v140
	v_add_u32_e32 v226, v201, v186
	s_nop 0
	s_nop 0
	s_nop 0
	s_nop 0
	s_nop 0
	s_nop 0
	s_nop 0
	s_nop 0
	s_nop 0
	s_nop 0
	s_nop 0
	s_nop 0
	s_nop 0
	s_nop 0
	v_mov_b32_e32 v24, v140
	v_mov_b32_e32 v25, v140
	v_mov_b32_e32 v26, v140
	v_mov_b32_e32 v27, v140
	v_mov_b32_e32 v28, v140
	v_mov_b32_e32 v29, v140
	v_mov_b32_e32 v30, v140
	v_mov_b32_e32 v31, v140
	v_mov_b32_e32 v32, v140
	v_mov_b32_e32 v33, v140
	v_mov_b64_e32 v[50:51], v[98:99]
	v_mov_b64_e32 v[52:53], v[100:101]
	v_mov_b64_e32 v[54:55], v[102:103]
	v_mov_b64_e32 v[56:57], v[104:105]
	v_mov_b64_e32 v[58:59], v[106:107]
	v_mov_b64_e32 v[60:61], v[108:109]
	v_mov_b64_e32 v[62:63], v[110:111]
	v_mov_b64_e32 v[64:65], v[112:113]
	s_mov_b32 s32, 0
	v_readlane_b32 s72, v249, 50
	s_cmp_gt_i32 s72, 7
	s_cbranch_scc1 .LBB0_2422
	s_mul_i32 s72, s72, 48
	v_readlane_b32 s73, v248, 47
	s_add_i32 s72, s73, s72
	v_readlane_b32 s78, v248, 48
	s_add_i32 s73, s72, 48
	s_min_i32 s78, s78, s73
	s_min_i32 s78, s78, 0x1be90
	v_readlane_b32 s84, v249, 16
	s_add_i32 s73, s72, s84
	s_cmp_ge_i32 s73, s78
	s_cbranch_scc1 .LBB0_2422
	v_writelane_b32 v244, s78, 3
	s_lshl_b32 s84, s84, 11
	s_add_i32 s84, s84, 0x24000
	v_and_b32_e32 v82, 63, v0
	v_and_b32_e32 v83, 31, v82
	v_lshrrev_b32_e32 v84, 5, v82
	v_lshlrev_b32_e32 v84, 10, v84
	v_lshl_add_u32 v83, v83, 2, v84
	v_add_u32_e32 v245, s84, v83
	s_mov_b32 s85, 2
	s_mov_b32 s32, 0x30
	s_branch .Lbgn_dec

.Lcvdc_go:
	v_add_u32_e32 v89, s72, v84
	v_add_u32_e32 v90, 1040, v89
	ds_read2_b32 v[4:5], v89 offset0:0 offset1:32
	ds_read2_b32 v[6:7], v89 offset0:64 offset1:96
	ds_read2_b32 v[8:9], v89 offset0:128 offset1:160
	ds_read2_b32 v[10:11], v89 offset0:192 offset1:224
	ds_read2_b32 v[12:13], v90 offset0:0 offset1:32
	ds_read2_b32 v[14:15], v90 offset0:64 offset1:96
	ds_read2_b32 v[16:17], v90 offset0:128 offset1:160
	ds_read2_b32 v[18:19], v90 offset0:192 offset1:224
	ds_read2_b32 v[20:21], v89 offset0:16 offset1:48
	ds_read2_b32 v[22:23], v89 offset0:80 offset1:112
	ds_read2_b32 v[24:25], v89 offset0:144 offset1:176
	ds_read2_b32 v[26:27], v89 offset0:208 offset1:240
	ds_read2_b32 v[28:29], v90 offset0:16 offset1:48
	ds_read2_b32 v[30:31], v90 offset0:80 offset1:112
	ds_read2_b32 v[32:33], v90 offset0:144 offset1:176
	ds_read2_b32 v[34:35], v90 offset0:208 offset1:240
	s_cmp_eq_u32 s98, 0
	s_cselect_b64 vcc, -1, 0
	s_movk_i32 s7, 0x2000
	s_cselect_b32 s7, 0x8000, s7
	v_cndmask_b32_e32 v91, v87, v86, vcc
	s_waitcnt lgkmcnt(8)
	v_pk_mul_f32 v[4:5], v[4:5], v[100:101]
	v_pk_mul_f32 v[6:7], v[6:7], v[100:101]
	v_pk_mul_f32 v[8:9], v[8:9], v[100:101]
	v_pk_mul_f32 v[10:11], v[10:11], v[100:101]
	v_pk_mul_f32 v[12:13], v[12:13], v[100:101]
	v_pk_mul_f32 v[14:15], v[14:15], v[100:101]
	v_pk_mul_f32 v[16:17], v[16:17], v[100:101]
	v_pk_mul_f32 v[18:19], v[18:19], v[100:101]
	v_cvt_pk_fp8_f32 v92, v4, v5
	v_cvt_pk_fp8_f32 v93, v8, v9
	v_cvt_pk_fp8_f32 v94, v12, v13
	v_cvt_pk_fp8_f32 v95, v16, v17
	v_cvt_pk_fp8_f32 v92, v6, v7 op_sel:[0,0,1]
	v_cvt_pk_fp8_f32 v93, v10, v11 op_sel:[0,0,1]
	v_cvt_pk_fp8_f32 v94, v14, v15 op_sel:[0,0,1]
	v_cvt_pk_fp8_f32 v95, v18, v19 op_sel:[0,0,1]
	global_store_dwordx4 v91, v[92:95], s[84:85] nt
	s_waitcnt lgkmcnt(0)
	v_pk_mul_f32 v[20:21], v[20:21], v[100:101]
	v_pk_mul_f32 v[22:23], v[22:23], v[100:101]
	v_pk_mul_f32 v[24:25], v[24:25], v[100:101]
	v_pk_mul_f32 v[26:27], v[26:27], v[100:101]
	v_pk_mul_f32 v[28:29], v[28:29], v[100:101]
	v_pk_mul_f32 v[30:31], v[30:31], v[100:101]
	v_pk_mul_f32 v[32:33], v[32:33], v[100:101]
	v_pk_mul_f32 v[34:35], v[34:35], v[100:101]
	v_cvt_pk_fp8_f32 v96, v20, v21
	v_cvt_pk_fp8_f32 v97, v24, v25
	v_cvt_pk_fp8_f32 v98, v28, v29
	v_cvt_pk_fp8_f32 v99, v32, v33
	v_cvt_pk_fp8_f32 v96, v22, v23 op_sel:[0,0,1]
	v_cvt_pk_fp8_f32 v97, v26, v27 op_sel:[0,0,1]
	v_cvt_pk_fp8_f32 v98, v30, v31 op_sel:[0,0,1]
	v_cvt_pk_fp8_f32 v99, v34, v35 op_sel:[0,0,1]
	s_add_u32 s84, s84, s7
	s_addc_u32 s85, s85, 0
	global_store_dwordx4 v91, v[96:99], s[84:85] nt
	s_mov_b32 s32, 1
	s_cmp_eq_u32 s13, 0
	s_cbranch_scc1 .LBB0_2858
	s_mov_b32 s25, s12
	s_mov_b32 s7, s72
	s_mov_b32 s72, s86
	s_mov_b32 s86, s7
	s_branch .Lcvdc_loop
	s_nop 0
	s_nop 0
	s_nop 0
	s_nop 0
	s_nop 0
	s_nop 0
	s_nop 0
	s_nop 0
	s_nop 0
	s_nop 0
	s_nop 0
	s_nop 0
	s_nop 0
	s_nop 0
